# same batched layer-0 residual loads, plus 96 bytes of skipped padding after the epilogue so the code that follows keeps its previous 256-byte alignment
# speedup vs baseline: 1.0092x; 1.0055x over previous
; __device__ __forceinline__ unsigned xb_ld(unsigned* p)              { return __hip_atomic_load(p, __ATOMIC_RELAXED, __HIP_MEMORY_SCOPE_AGENT); }
; __device__ __forceinline__ unsigned xb_add(unsigned* p, unsigned v) { return __hip_atomic_fetch_add(p, v, __ATOMIC_RELAXED, __HIP_MEMORY_SCOPE_AGENT); }
; #define XB_SPIN(cond, bar) do { unsigned _sp = 0; while (cond) { __builtin_amdgcn_s_sleep(1); \
;     if ((++_sp & 255u) == 0u) { if (xb_ld(&(bar)[XB_TMO])) break; if (_sp > XB_SPIN_CAP) { atomicAdd(&(bar)[XB_TMO], 1u); break; } } } } while (0)
; __device__ __forceinline__ void xcd_barrier(const XcdBarrier& b, int wave) {
;     ...
;         const unsigned old = xb_add(&bar[XB_XSUB(b.x)], 1u);
;         const unsigned gen = old / nloc;
;         if (old + 1u == (gen + 1u) * nloc) {
;             __builtin_amdgcn_fence(__ATOMIC_RELEASE, "agent");
;             asm volatile("s_waitcnt vmcnt(0)" ::: "memory");
;             const unsigned og = xb_add(&bar[XB_TOP], 1u);
;             const unsigned tg = og / nx;
;             if (og + 1u == (tg + 1u) * nx) xb_add(&bar[XB_TOPGEN], 1u);
;             else XB_SPIN(xb_ld(&bar[XB_TOPGEN]) == tg, bar);
;             __builtin_amdgcn_fence(__ATOMIC_ACQUIRE, "agent");
;             xb_add(&bar[XB_XGEN(b.x)], 1u);
;             asm volatile("s_waitcnt vmcnt(0)" ::: "memory");
.LBB0_924:
	s_or_b64 exec, exec, s[2:3]
	v_readlane_b32 s2, v253, 38
	v_readlane_b32 s3, v253, 39
	s_waitcnt vmcnt(0)
	buffer_inv sc1
	s_nop 2
	global_atomic_add v185, v213, s[2:3]
	s_waitcnt vmcnt(0)
	s_branch .LBB0_925
	s_nop 0
	s_nop 0
	s_nop 0
	s_nop 0
	s_nop 0
	s_nop 0
	s_nop 0
	s_nop 0
	s_nop 0
	s_nop 0
	s_nop 0
	s_nop 0
	s_nop 0
	s_nop 0
	s_nop 0
	s_nop 0
	s_nop 0
	s_nop 0
	s_nop 0
	s_nop 0
	s_nop 0
	s_nop 0
	s_nop 0
